# stack7_nt + non-temporal hint on the in-projection epilogue stores
# baseline (speedup 1.0000x reference)
; __device__ __forceinline__ unsigned cvt_pk_bf16(float lo, float hi) { const f32x2 v = {lo, hi}; return __builtin_bit_cast(unsigned, __builtin_convertvector(v, bf16x2_t)); }
;     __device__ __forceinline__ void operator()(g8::Acc& acc, const g8::Unit& u, int wr, int wc, int fr, int fq) const {
;     ...
;         const bool isq = pn < 8;
;         const int head = 2 * ((pn - 4) & 3) + (wc >> 1);
;         const int dd0 = 32 * (wc & 1) + 8 * fq;
;         const int colbase = (isq ? 1024 : 2048) + head * 128 + dd0;
;         const float lg2 = log2f(1.0f - exp2f(-5.0f - (float)head));
;         float fr_[8];
; #pragma unroll
;         for (int t = 0; t < 8; ++t) fr_[t] = exp2f(-(float)(dd0 + t) * 0.20762050593046014f) * 0.15915494309189535f;
; #pragma unroll
;         for (int ai = 0; ai < 2; ++ai)
; #pragma unroll
;             for (int m = 0; m < 4; ++m) {
;                 const int row = row0 + ai * 128 + m * 16, pos = row & 2047, i = wr * 64 + m * 16 + fr;
;                 const float sc = isq ? exp2f(lg2 * (float)i) : exp2f(-lg2 * (float)i) * 0.08838834764831845f;
;                 const float fp = (float)pos;
;                 float o1[8], o2[8];
; #pragma unroll
;                 for (int t = 0; t < 8; ++t) {
;                     const float rev = __builtin_amdgcn_fractf(fp * fr_[t]);
;                     const float cs = __builtin_amdgcn_cosf(rev) * sc, sn = __builtin_amdgcn_sinf(rev) * sc;
;                     const float a = acc[ai][0][m][t >> 2][t & 3], b = acc[ai][1][m][t >> 2][t & 3];
;                     o1[t] = a * cs - b * sn; o2[t] = b * cs + a * sn;
;                 }
;                 bf16_t* rowp = O + (size_t)row * NPROJ + colbase;
;                 u32x4 w1, w2; w1.x = cvt_pk_bf16(o1[0], o1[1]); w1.y = cvt_pk_bf16(o1[2], o1[3]); w1.z = cvt_pk_bf16(o1[4], o1[5]); w1.w = cvt_pk_bf16(o1[6], o1[7]);
;                 w2.x = cvt_pk_bf16(o2[0], o2[1]); w2.y = cvt_pk_bf16(o2[2], o2[3]); w2.z = cvt_pk_bf16(o2[4], o2[5]); w2.w = cvt_pk_bf16(o2[6], o2[7]);
;                 *(u32x4*)rowp = w1; *(u32x4*)(rowp + 64) = w2;
.LBB0_249:
	v_lshl_add_u32 v146, v132, 3, s72
	v_cvt_f32_u32_e32 v134, v146
	s_and_b64 s[0:1], s[6:7], exec
	s_movk_i32 s0, 0x400
	s_cselect_b32 s0, s0, 0x800
	v_mul_f32_e32 v135, 0xbe549a78, v134
	v_cmp_gt_f32_e32 vcc, s70, v135
	s_lshl_b32 s1, s57, 7
	s_or_b32 s0, s1, s0
	v_cndmask_b32_e32 v135, 0, v206, vcc
	v_fmac_f32_e32 v135, 0xbe549a78, v134
	v_exp_f32_e32 v134, v135
	v_cndmask_b32_e32 v135, 0, v208, vcc
	v_add_u32_e32 v164, s0, v146
	v_lshlrev_b32_e32 v194, 1, v164
	v_ldexp_f32 v134, v134, v135
	v_or_b32_e32 v135, 1, v146
	v_cvt_f32_u32_e32 v135, v135
	v_mul_f32_e32 v134, 0.15915494, v134
	s_mov_b64 s[46:47], -1
	v_mul_f32_e32 v136, 0xbe549a78, v135
	v_cmp_gt_f32_e32 vcc, s70, v136
	s_nop 1
	v_cndmask_b32_e32 v136, 0, v206, vcc
	v_fmac_f32_e32 v136, 0xbe549a78, v135
	v_exp_f32_e32 v135, v136
	v_cndmask_b32_e32 v136, 0, v208, vcc
	v_ldexp_f32 v135, v135, v136
	v_mul_f32_e32 v136, 0.15915494, v135
	v_or_b32_e32 v135, 2, v146
	v_cvt_f32_u32_e32 v135, v135
	v_mul_f32_e32 v137, 0xbe549a78, v135
	v_cmp_gt_f32_e32 vcc, s70, v137
	s_nop 1
	v_cndmask_b32_e32 v137, 0, v206, vcc
	v_fmac_f32_e32 v137, 0xbe549a78, v135
	v_exp_f32_e32 v135, v137
	v_cndmask_b32_e32 v137, 0, v208, vcc
	v_ldexp_f32 v135, v135, v137
	v_or_b32_e32 v137, 3, v146
	v_cvt_f32_u32_e32 v137, v137
	v_mul_f32_e32 v135, 0.15915494, v135
	v_mul_f32_e32 v138, 0xbe549a78, v137
	v_cmp_gt_f32_e32 vcc, s70, v138
	s_nop 1
	v_cndmask_b32_e32 v138, 0, v206, vcc
	v_fmac_f32_e32 v138, 0xbe549a78, v137
	v_exp_f32_e32 v137, v138
	v_cndmask_b32_e32 v138, 0, v208, vcc
	v_ldexp_f32 v137, v137, v138
	v_or_b32_e32 v138, 4, v146
	v_cvt_f32_u32_e32 v138, v138
	v_mul_f32_e32 v137, 0.15915494, v137
	v_mul_f32_e32 v139, 0xbe549a78, v138
	v_cmp_gt_f32_e32 vcc, s70, v139
	s_nop 1
	v_cndmask_b32_e32 v139, 0, v206, vcc
	v_fmac_f32_e32 v139, 0xbe549a78, v138
	v_exp_f32_e32 v138, v139
	v_cndmask_b32_e32 v139, 0, v208, vcc
	v_ldexp_f32 v138, v138, v139
	v_or_b32_e32 v139, 5, v146
	v_cvt_f32_u32_e32 v139, v139
	v_mul_f32_e32 v138, 0.15915494, v138
	v_mul_f32_e32 v140, 0xbe549a78, v139
	v_cmp_gt_f32_e32 vcc, s70, v140
	s_nop 1
	v_cndmask_b32_e32 v140, 0, v206, vcc
	v_fmac_f32_e32 v140, 0xbe549a78, v139
	v_exp_f32_e32 v139, v140
	v_cndmask_b32_e32 v140, 0, v208, vcc
	v_ldexp_f32 v139, v139, v140
	v_or_b32_e32 v140, 6, v146
	v_cvt_f32_u32_e32 v140, v140
	v_mul_f32_e32 v139, 0.15915494, v139
	v_mul_f32_e32 v141, 0xbe549a78, v140
	v_cmp_gt_f32_e32 vcc, s70, v141
	s_nop 1
	v_cndmask_b32_e32 v141, 0, v206, vcc
	v_fmac_f32_e32 v141, 0xbe549a78, v140
	v_exp_f32_e32 v140, v141
	v_cndmask_b32_e32 v141, 0, v208, vcc
	v_ldexp_f32 v140, v140, v141
	v_or_b32_e32 v141, 7, v146
	v_cvt_f32_u32_e32 v141, v141
	v_and_b32_e32 v146, 0x7cf, v131
	v_cvt_f32_u32_e32 v161, v146
	v_mul_f32_e32 v140, 0.15915494, v140
	v_mul_f32_e32 v147, 0xbe549a78, v141
	v_cmp_gt_f32_e32 vcc, s70, v147
	v_mul_f32_e32 v146, v134, v161
	s_nop 0
	v_cndmask_b32_e32 v147, 0, v206, vcc
	v_fmac_f32_e32 v147, 0xbe549a78, v141
	v_exp_f32_e32 v141, v147
	v_cndmask_b32_e32 v147, 0, v208, vcc
	s_andn2_b64 vcc, exec, s[42:43]
	v_ldexp_f32 v141, v141, v147
	v_fract_f32_e32 v147, v146
	v_cos_f32_e32 v146, v147
	v_sin_f32_e32 v148, v147
	v_mul_f32_e32 v147, v136, v161
	v_fract_f32_e32 v149, v147
	v_cos_f32_e32 v147, v149
	v_sin_f32_e32 v149, v149
	v_mul_f32_e32 v141, 0.15915494, v141
	v_pk_mul_f32 v[146:147], v[146:147], v[130:131] op_sel_hi:[1,0]
	v_pk_mul_f32 v[148:149], v[148:149], v[130:131] op_sel_hi:[1,0]
	v_pk_mul_f32 v[150:151], v[94:95], v[146:147]
	s_nop 0
	v_pk_fma_f32 v[150:151], v[126:127], v[148:149], v[150:151]
	v_pk_mul_f32 v[148:149], v[94:95], v[148:149]
	v_cvt_pk_bf16_f32 v150, v150, v151
	v_pk_fma_f32 v[146:147], v[126:127], v[146:147], v[148:149] neg_lo:[0,0,1] neg_hi:[0,0,1]
	v_mul_f32_e32 v148, v135, v161
	v_fract_f32_e32 v149, v148
	v_cos_f32_e32 v148, v149
	v_sin_f32_e32 v152, v149
	v_mul_f32_e32 v149, v137, v161
	v_fract_f32_e32 v153, v149
	v_cos_f32_e32 v149, v153
	v_sin_f32_e32 v153, v153
	v_cvt_pk_bf16_f32 v146, v146, v147
	v_pk_mul_f32 v[148:149], v[148:149], v[130:131] op_sel_hi:[1,0]
	v_pk_mul_f32 v[152:153], v[152:153], v[130:131] op_sel_hi:[1,0]
	v_pk_mul_f32 v[154:155], v[96:97], v[148:149]
	s_nop 0
	v_pk_fma_f32 v[154:155], v[128:129], v[152:153], v[154:155]
	v_pk_mul_f32 v[152:153], v[96:97], v[152:153]
	v_cvt_pk_bf16_f32 v151, v154, v155
	v_pk_fma_f32 v[148:149], v[128:129], v[148:149], v[152:153] neg_lo:[0,0,1] neg_hi:[0,0,1]
	v_mul_f32_e32 v152, v138, v161
	v_fract_f32_e32 v153, v152
	v_cos_f32_e32 v152, v153
	v_sin_f32_e32 v156, v153
	v_mul_f32_e32 v153, v139, v161
	v_fract_f32_e32 v157, v153
	v_cos_f32_e32 v153, v157
	v_sin_f32_e32 v157, v157
	v_cvt_pk_bf16_f32 v147, v148, v149
	v_pk_mul_f32 v[152:153], v[152:153], v[130:131] op_sel_hi:[1,0]
	v_pk_mul_f32 v[156:157], v[156:157], v[130:131] op_sel_hi:[1,0]
	v_pk_mul_f32 v[158:159], v[90:91], v[152:153]
	s_nop 0
	v_pk_fma_f32 v[158:159], v[122:123], v[156:157], v[158:159]
	v_pk_mul_f32 v[156:157], v[90:91], v[156:157]
	s_nop 0
	v_pk_fma_f32 v[152:153], v[122:123], v[152:153], v[156:157] neg_lo:[0,0,1] neg_hi:[0,0,1]
	v_mul_f32_e32 v156, v140, v161
	v_fract_f32_e32 v157, v156
	v_cos_f32_e32 v156, v157
	v_sin_f32_e32 v160, v157
	v_mul_f32_e32 v157, v141, v161
	v_fract_f32_e32 v161, v157
	v_cos_f32_e32 v157, v161
	v_sin_f32_e32 v161, v161
	v_cvt_pk_bf16_f32 v148, v152, v153
	v_cvt_pk_bf16_f32 v152, v158, v159
	v_pk_mul_f32 v[156:157], v[156:157], v[130:131] op_sel_hi:[1,0]
	v_pk_mul_f32 v[160:161], v[160:161], v[130:131] op_sel_hi:[1,0]
	v_pk_mul_f32 v[162:163], v[92:93], v[156:157]
	v_or_b32_e32 v130, 16, v145
	v_pk_fma_f32 v[162:163], v[124:125], v[160:161], v[162:163]
	v_pk_mul_f32 v[160:161], v[92:93], v[160:161]
	v_cvt_pk_bf16_f32 v153, v162, v163
	v_pk_fma_f32 v[156:157], v[124:125], v[156:157], v[160:161] neg_lo:[0,0,1] neg_hi:[0,0,1]
	v_mov_b64_e32 v[160:161], s[10:11]
	v_mad_i64_i32 v[160:161], s[0:1], v131, s71, v[160:161]
	v_lshl_add_u64 v[160:161], v[160:161], 0, v[194:195]
	v_cvt_pk_bf16_f32 v149, v156, v157
	global_store_dwordx4 v[160:161], v[146:149], off nt
	global_store_dwordx4 v[160:161], v[150:153], off offset:128 nt
	s_nop 0
	v_cvt_f32_u32_e32 v146, v130
	v_cndmask_b32_e64 v130, 0, 1, s[42:43]
	v_cmp_ne_u32_e64 s[6:7], 1, v130
	v_mul_f32_e64 v148, -v133, v146
	v_cmp_gt_f32_e64 s[0:1], s70, v148
	s_cbranch_vccnz .LBB0_251
	s_nop 0
	v_cndmask_b32_e64 v130, 0, v206, s[0:1]
	v_fma_f32 v130, -v133, v146, v130
	v_exp_f32_e32 v130, v130
	v_cndmask_b32_e64 v147, 0, v208, s[0:1]
	s_mov_b64 s[46:47], 0
	v_ldexp_f32 v130, v130, v147
	v_mul_f32_e32 v130, 0x3db504f3, v130

; __device__ __forceinline__ unsigned cvt_pk_bf16(float lo, float hi) { const f32x2 v = {lo, hi}; return __builtin_bit_cast(unsigned, __builtin_convertvector(v, bf16x2_t)); }
;     __device__ __forceinline__ void operator()(g8::Acc& acc, const g8::Unit& u, int wr, int wc, int fr, int fq) const {
;     ...
;         for (int ai = 0; ai < 2; ++ai)
; #pragma unroll
;             for (int m = 0; m < 4; ++m) {
;                 const int row = row0 + ai * 128 + m * 16, pos = row & 2047, i = wr * 64 + m * 16 + fr;
;                 const float sc = isq ? exp2f(lg2 * (float)i) : exp2f(-lg2 * (float)i) * 0.08838834764831845f;
;                 const float fp = (float)pos;
;                 float o1[8], o2[8];
; #pragma unroll
;                 for (int t = 0; t < 8; ++t) {
;                     const float rev = __builtin_amdgcn_fractf(fp * fr_[t]);
;                     const float cs = __builtin_amdgcn_cosf(rev) * sc, sn = __builtin_amdgcn_sinf(rev) * sc;
;                     const float a = acc[ai][0][m][t >> 2][t & 3], b = acc[ai][1][m][t >> 2][t & 3];
;                     o1[t] = a * cs - b * sn; o2[t] = b * cs + a * sn;
;                 }
;                 bf16_t* rowp = O + (size_t)row * NPROJ + colbase;
;                 u32x4 w1, w2; w1.x = cvt_pk_bf16(o1[0], o1[1]); w1.y = cvt_pk_bf16(o1[2], o1[3]); w1.z = cvt_pk_bf16(o1[4], o1[5]); w1.w = cvt_pk_bf16(o1[6], o1[7]);
;                 w2.x = cvt_pk_bf16(o2[0], o2[1]); w2.y = cvt_pk_bf16(o2[2], o2[3]); w2.z = cvt_pk_bf16(o2[4], o2[5]); w2.w = cvt_pk_bf16(o2[6], o2[7]);
;                 *(u32x4*)rowp = w1; *(u32x4*)(rowp + 64) = w2;
.LBB0_253:
	s_movk_i32 s0, 0x7df
	v_bitop3_b32 v150, v131, s0, 16 bitop3:0xc8
	v_cvt_f32_u32_e32 v165, v150
	v_or_b32_e32 v147, 16, v131
	s_mov_b64 s[42:43], -1
	s_and_b64 vcc, exec, s[6:7]
	v_mul_f32_e32 v150, v134, v165
	v_fract_f32_e32 v151, v150
	v_cos_f32_e32 v150, v151
	v_sin_f32_e32 v152, v151
	v_mul_f32_e32 v151, v136, v165
	v_fract_f32_e32 v153, v151
	v_cos_f32_e32 v151, v153
	v_sin_f32_e32 v153, v153
	v_pk_mul_f32 v[150:151], v[150:151], v[130:131] op_sel_hi:[1,0]
	v_pk_mul_f32 v[152:153], v[152:153], v[130:131] op_sel_hi:[1,0]
	v_pk_mul_f32 v[154:155], v[86:87], v[150:151]
	s_nop 0
	v_pk_fma_f32 v[154:155], v[118:119], v[152:153], v[154:155]
	v_pk_mul_f32 v[152:153], v[86:87], v[152:153]
	v_cvt_pk_bf16_f32 v154, v154, v155
	v_pk_fma_f32 v[150:151], v[118:119], v[150:151], v[152:153] neg_lo:[0,0,1] neg_hi:[0,0,1]
	v_mul_f32_e32 v152, v135, v165
	v_fract_f32_e32 v153, v152
	v_cos_f32_e32 v152, v153
	v_sin_f32_e32 v156, v153
	v_mul_f32_e32 v153, v137, v165
	v_fract_f32_e32 v157, v153
	v_cos_f32_e32 v153, v157
	v_sin_f32_e32 v157, v157
	v_cvt_pk_bf16_f32 v150, v150, v151
	v_pk_mul_f32 v[152:153], v[152:153], v[130:131] op_sel_hi:[1,0]
	v_pk_mul_f32 v[156:157], v[156:157], v[130:131] op_sel_hi:[1,0]
	v_pk_mul_f32 v[158:159], v[88:89], v[152:153]
	s_nop 0
	v_pk_fma_f32 v[158:159], v[120:121], v[156:157], v[158:159]
	v_pk_mul_f32 v[156:157], v[88:89], v[156:157]
	v_cvt_pk_bf16_f32 v155, v158, v159
	v_pk_fma_f32 v[152:153], v[120:121], v[152:153], v[156:157] neg_lo:[0,0,1] neg_hi:[0,0,1]
	v_mul_f32_e32 v156, v138, v165
	v_fract_f32_e32 v157, v156
	v_cos_f32_e32 v156, v157
	v_sin_f32_e32 v160, v157
	v_mul_f32_e32 v157, v139, v165
	v_fract_f32_e32 v161, v157
	v_cos_f32_e32 v157, v161
	v_sin_f32_e32 v161, v161
	v_cvt_pk_bf16_f32 v151, v152, v153
	v_pk_mul_f32 v[156:157], v[156:157], v[130:131] op_sel_hi:[1,0]
	v_pk_mul_f32 v[160:161], v[160:161], v[130:131] op_sel_hi:[1,0]
	v_pk_mul_f32 v[162:163], v[82:83], v[156:157]
	s_nop 0
	v_pk_fma_f32 v[162:163], v[114:115], v[160:161], v[162:163]
	v_pk_mul_f32 v[160:161], v[82:83], v[160:161]
	s_nop 0
	v_pk_fma_f32 v[156:157], v[114:115], v[156:157], v[160:161] neg_lo:[0,0,1] neg_hi:[0,0,1]
	v_mul_f32_e32 v160, v140, v165
	v_fract_f32_e32 v161, v160
	v_cos_f32_e32 v160, v161
	v_sin_f32_e32 v164, v161
	v_mul_f32_e32 v161, v141, v165
	v_fract_f32_e32 v165, v161
	v_cos_f32_e32 v161, v165
	v_sin_f32_e32 v165, v165
	v_cvt_pk_bf16_f32 v152, v156, v157
	v_cvt_pk_bf16_f32 v156, v162, v163
	v_pk_mul_f32 v[160:161], v[160:161], v[130:131] op_sel_hi:[1,0]
	v_pk_mul_f32 v[164:165], v[164:165], v[130:131] op_sel_hi:[1,0]
	v_pk_mul_f32 v[166:167], v[84:85], v[160:161]
	v_or_b32_e32 v130, 32, v145
	v_pk_fma_f32 v[166:167], v[116:117], v[164:165], v[166:167]
	v_pk_mul_f32 v[164:165], v[84:85], v[164:165]
	v_cvt_pk_bf16_f32 v157, v166, v167
	v_pk_fma_f32 v[160:161], v[116:117], v[160:161], v[164:165] neg_lo:[0,0,1] neg_hi:[0,0,1]
	v_mov_b64_e32 v[164:165], s[10:11]
	v_mad_i64_i32 v[164:165], s[0:1], v147, s71, v[164:165]
	v_cvt_f32_u32_e32 v147, v130
	v_lshl_add_u64 v[164:165], v[164:165], 0, v[194:195]
	v_cvt_pk_bf16_f32 v153, v160, v161
	global_store_dwordx4 v[164:165], v[150:153], off nt
	global_store_dwordx4 v[164:165], v[154:157], off offset:128 nt
	s_nop 0
	v_mul_f32_e64 v150, -v133, v147
	v_cmp_gt_f32_e64 s[0:1], s70, v150
	s_cbranch_vccnz .LBB0_255
	s_nop 0
	v_cndmask_b32_e64 v130, 0, v206, s[0:1]
	v_fma_f32 v130, -v133, v147, v130
	v_exp_f32_e32 v130, v130
	v_cndmask_b32_e64 v151, 0, v208, s[0:1]
	s_mov_b64 s[42:43], 0
	v_ldexp_f32 v130, v130, v151
	v_mul_f32_e32 v130, 0x3db504f3, v130

; __device__ __forceinline__ unsigned cvt_pk_bf16(float lo, float hi) { const f32x2 v = {lo, hi}; return __builtin_bit_cast(unsigned, __builtin_convertvector(v, bf16x2_t)); }
;     __device__ __forceinline__ void operator()(g8::Acc& acc, const g8::Unit& u, int wr, int wc, int fr, int fq) const {
;     ...
;         for (int ai = 0; ai < 2; ++ai)
; #pragma unroll
;             for (int m = 0; m < 4; ++m) {
;                 const int row = row0 + ai * 128 + m * 16, pos = row & 2047, i = wr * 64 + m * 16 + fr;
;                 const float sc = isq ? exp2f(lg2 * (float)i) : exp2f(-lg2 * (float)i) * 0.08838834764831845f;
;                 const float fp = (float)pos;
;                 float o1[8], o2[8];
; #pragma unroll
;                 for (int t = 0; t < 8; ++t) {
;                     const float rev = __builtin_amdgcn_fractf(fp * fr_[t]);
;                     const float cs = __builtin_amdgcn_cosf(rev) * sc, sn = __builtin_amdgcn_sinf(rev) * sc;
;                     const float a = acc[ai][0][m][t >> 2][t & 3], b = acc[ai][1][m][t >> 2][t & 3];
;                     o1[t] = a * cs - b * sn; o2[t] = b * cs + a * sn;
;                 }
;                 bf16_t* rowp = O + (size_t)row * NPROJ + colbase;
;                 u32x4 w1, w2; w1.x = cvt_pk_bf16(o1[0], o1[1]); w1.y = cvt_pk_bf16(o1[2], o1[3]); w1.z = cvt_pk_bf16(o1[4], o1[5]); w1.w = cvt_pk_bf16(o1[6], o1[7]);
;                 w2.x = cvt_pk_bf16(o2[0], o2[1]); w2.y = cvt_pk_bf16(o2[2], o2[3]); w2.z = cvt_pk_bf16(o2[4], o2[5]); w2.w = cvt_pk_bf16(o2[6], o2[7]);
;                 *(u32x4*)rowp = w1; *(u32x4*)(rowp + 64) = w2;
.LBB0_257:
	s_movk_i32 s0, 0x7ef
	v_bitop3_b32 v152, v131, s0, 32 bitop3:0xc8
	v_cvt_f32_u32_e32 v167, v152
	v_or_b32_e32 v170, 32, v131
	s_mov_b64 s[42:43], -1
	s_and_b64 vcc, exec, s[6:7]
	v_mul_f32_e32 v152, v134, v167
	v_fract_f32_e32 v153, v152
	v_cos_f32_e32 v152, v153
	v_sin_f32_e32 v154, v153
	v_mul_f32_e32 v153, v136, v167
	v_fract_f32_e32 v155, v153
	v_cos_f32_e32 v153, v155
	v_sin_f32_e32 v155, v155
	v_pk_mul_f32 v[152:153], v[152:153], v[130:131] op_sel_hi:[1,0]
	v_pk_mul_f32 v[154:155], v[154:155], v[130:131] op_sel_hi:[1,0]
	v_pk_mul_f32 v[156:157], v[78:79], v[152:153]
	s_nop 0
	v_pk_fma_f32 v[156:157], v[110:111], v[154:155], v[156:157]
	v_pk_mul_f32 v[154:155], v[78:79], v[154:155]
	v_cvt_pk_bf16_f32 v156, v156, v157
	v_pk_fma_f32 v[152:153], v[110:111], v[152:153], v[154:155] neg_lo:[0,0,1] neg_hi:[0,0,1]
	v_mul_f32_e32 v154, v135, v167
	v_fract_f32_e32 v155, v154
	v_cos_f32_e32 v154, v155
	v_sin_f32_e32 v158, v155
	v_mul_f32_e32 v155, v137, v167
	v_fract_f32_e32 v159, v155
	v_cos_f32_e32 v155, v159
	v_sin_f32_e32 v159, v159
	v_cvt_pk_bf16_f32 v152, v152, v153
	v_pk_mul_f32 v[154:155], v[154:155], v[130:131] op_sel_hi:[1,0]
	v_pk_mul_f32 v[158:159], v[158:159], v[130:131] op_sel_hi:[1,0]
	v_pk_mul_f32 v[160:161], v[80:81], v[154:155]
	s_nop 0
	v_pk_fma_f32 v[160:161], v[112:113], v[158:159], v[160:161]
	v_pk_mul_f32 v[158:159], v[80:81], v[158:159]
	v_cvt_pk_bf16_f32 v157, v160, v161
	v_pk_fma_f32 v[154:155], v[112:113], v[154:155], v[158:159] neg_lo:[0,0,1] neg_hi:[0,0,1]
	v_mul_f32_e32 v158, v138, v167
	v_fract_f32_e32 v159, v158
	v_cos_f32_e32 v158, v159
	v_sin_f32_e32 v162, v159
	v_mul_f32_e32 v159, v139, v167
	v_fract_f32_e32 v163, v159
	v_cos_f32_e32 v159, v163
	v_sin_f32_e32 v163, v163
	v_cvt_pk_bf16_f32 v153, v154, v155
	v_pk_mul_f32 v[158:159], v[158:159], v[130:131] op_sel_hi:[1,0]
	v_pk_mul_f32 v[162:163], v[162:163], v[130:131] op_sel_hi:[1,0]
	v_pk_mul_f32 v[164:165], v[74:75], v[158:159]
	s_nop 0
	v_pk_fma_f32 v[164:165], v[106:107], v[162:163], v[164:165]
	v_pk_mul_f32 v[162:163], v[74:75], v[162:163]
	s_nop 0
	v_pk_fma_f32 v[158:159], v[106:107], v[158:159], v[162:163] neg_lo:[0,0,1] neg_hi:[0,0,1]
	v_mul_f32_e32 v162, v140, v167
	v_fract_f32_e32 v163, v162
	v_cos_f32_e32 v162, v163
	v_sin_f32_e32 v166, v163
	v_mul_f32_e32 v163, v141, v167
	v_fract_f32_e32 v167, v163
	v_cos_f32_e32 v163, v167
	v_sin_f32_e32 v167, v167
	v_cvt_pk_bf16_f32 v154, v158, v159
	v_cvt_pk_bf16_f32 v158, v164, v165
	v_pk_mul_f32 v[162:163], v[162:163], v[130:131] op_sel_hi:[1,0]
	v_pk_mul_f32 v[166:167], v[166:167], v[130:131] op_sel_hi:[1,0]
	v_pk_mul_f32 v[168:169], v[76:77], v[162:163]
	v_or_b32_e32 v130, 48, v145
	v_pk_fma_f32 v[168:169], v[108:109], v[166:167], v[168:169]
	v_pk_mul_f32 v[166:167], v[76:77], v[166:167]
	v_cvt_f32_u32_e32 v145, v130
	v_pk_fma_f32 v[162:163], v[108:109], v[162:163], v[166:167] neg_lo:[0,0,1] neg_hi:[0,0,1]
	v_mov_b64_e32 v[166:167], s[10:11]
	v_mad_i64_i32 v[166:167], s[0:1], v170, s71, v[166:167]
	v_lshl_add_u64 v[166:167], v[166:167], 0, v[194:195]
	v_cvt_pk_bf16_f32 v155, v162, v163
	v_cvt_pk_bf16_f32 v159, v168, v169
	global_store_dwordx4 v[166:167], v[152:155], off nt
	global_store_dwordx4 v[166:167], v[156:159], off offset:128 nt
	s_nop 0
	v_mul_f32_e64 v152, -v133, v145
	v_cmp_gt_f32_e64 s[0:1], s70, v152
	s_cbranch_vccnz .LBB0_259
	s_nop 0
	v_cndmask_b32_e64 v130, 0, v206, s[0:1]
	v_fma_f32 v130, -v133, v145, v130
	v_exp_f32_e32 v130, v130
	v_cndmask_b32_e64 v153, 0, v208, s[0:1]
	s_mov_b64 s[42:43], 0
	v_ldexp_f32 v130, v130, v153
	v_mul_f32_e32 v130, 0x3db504f3, v130

; __device__ __forceinline__ unsigned cvt_pk_bf16(float lo, float hi) { const f32x2 v = {lo, hi}; return __builtin_bit_cast(unsigned, __builtin_convertvector(v, bf16x2_t)); }
;     __device__ __forceinline__ void operator()(g8::Acc& acc, const g8::Unit& u, int wr, int wc, int fr, int fq) const {
;     ...
;         for (int ai = 0; ai < 2; ++ai)
; #pragma unroll
;             for (int m = 0; m < 4; ++m) {
;                 const int row = row0 + ai * 128 + m * 16, pos = row & 2047, i = wr * 64 + m * 16 + fr;
;                 const float sc = isq ? exp2f(lg2 * (float)i) : exp2f(-lg2 * (float)i) * 0.08838834764831845f;
;                 const float fp = (float)pos;
;                 float o1[8], o2[8];
; #pragma unroll
;                 for (int t = 0; t < 8; ++t) {
;                     const float rev = __builtin_amdgcn_fractf(fp * fr_[t]);
;                     const float cs = __builtin_amdgcn_cosf(rev) * sc, sn = __builtin_amdgcn_sinf(rev) * sc;
;                     const float a = acc[ai][0][m][t >> 2][t & 3], b = acc[ai][1][m][t >> 2][t & 3];
;                     o1[t] = a * cs - b * sn; o2[t] = b * cs + a * sn;
;                 }
;                 bf16_t* rowp = O + (size_t)row * NPROJ + colbase;
;                 u32x4 w1, w2; w1.x = cvt_pk_bf16(o1[0], o1[1]); w1.y = cvt_pk_bf16(o1[2], o1[3]); w1.z = cvt_pk_bf16(o1[4], o1[5]); w1.w = cvt_pk_bf16(o1[6], o1[7]);
;                 w2.x = cvt_pk_bf16(o2[0], o2[1]); w2.y = cvt_pk_bf16(o2[2], o2[3]); w2.z = cvt_pk_bf16(o2[4], o2[5]); w2.w = cvt_pk_bf16(o2[6], o2[7]);
;                 *(u32x4*)rowp = w1; *(u32x4*)(rowp + 64) = w2;
.LBB0_261:
	s_movk_i32 s0, 0x7ff
	v_bitop3_b32 v154, v131, s0, 48 bitop3:0xc8
	v_cvt_f32_u32_e32 v169, v154
	v_or_b32_e32 v172, 48, v131
	s_and_b64 vcc, exec, s[6:7]
	v_mul_f32_e32 v154, v134, v169
	v_fract_f32_e32 v155, v154
	v_cos_f32_e32 v154, v155
	v_sin_f32_e32 v156, v155
	v_mul_f32_e32 v155, v136, v169
	v_fract_f32_e32 v157, v155
	v_cos_f32_e32 v155, v157
	v_sin_f32_e32 v157, v157
	v_pk_mul_f32 v[154:155], v[154:155], v[130:131] op_sel_hi:[1,0]
	v_pk_mul_f32 v[156:157], v[156:157], v[130:131] op_sel_hi:[1,0]
	v_pk_mul_f32 v[158:159], v[70:71], v[154:155]
	s_nop 0
	v_pk_fma_f32 v[158:159], v[102:103], v[156:157], v[158:159]
	v_pk_mul_f32 v[156:157], v[70:71], v[156:157]
	v_cvt_pk_bf16_f32 v158, v158, v159
	v_pk_fma_f32 v[154:155], v[102:103], v[154:155], v[156:157] neg_lo:[0,0,1] neg_hi:[0,0,1]
	v_mul_f32_e32 v156, v135, v169
	v_fract_f32_e32 v157, v156
	v_cos_f32_e32 v156, v157
	v_sin_f32_e32 v160, v157
	v_mul_f32_e32 v157, v137, v169
	v_fract_f32_e32 v161, v157
	v_cos_f32_e32 v157, v161
	v_sin_f32_e32 v161, v161
	v_cvt_pk_bf16_f32 v154, v154, v155
	v_pk_mul_f32 v[156:157], v[156:157], v[130:131] op_sel_hi:[1,0]
	v_pk_mul_f32 v[160:161], v[160:161], v[130:131] op_sel_hi:[1,0]
	v_pk_mul_f32 v[162:163], v[72:73], v[156:157]
	s_nop 0
	v_pk_fma_f32 v[162:163], v[104:105], v[160:161], v[162:163]
	v_pk_mul_f32 v[160:161], v[72:73], v[160:161]
	v_cvt_pk_bf16_f32 v159, v162, v163
	v_pk_fma_f32 v[156:157], v[104:105], v[156:157], v[160:161] neg_lo:[0,0,1] neg_hi:[0,0,1]
	v_mul_f32_e32 v160, v138, v169
	v_fract_f32_e32 v161, v160
	v_cos_f32_e32 v160, v161
	v_sin_f32_e32 v164, v161
	v_mul_f32_e32 v161, v139, v169
	v_fract_f32_e32 v165, v161
	v_cos_f32_e32 v161, v165
	v_sin_f32_e32 v165, v165
	v_cvt_pk_bf16_f32 v155, v156, v157
	v_pk_mul_f32 v[160:161], v[160:161], v[130:131] op_sel_hi:[1,0]
	v_pk_mul_f32 v[164:165], v[164:165], v[130:131] op_sel_hi:[1,0]
	v_pk_mul_f32 v[166:167], v[66:67], v[160:161]
	s_nop 0
	v_pk_fma_f32 v[166:167], v[98:99], v[164:165], v[166:167]
	v_pk_mul_f32 v[164:165], v[66:67], v[164:165]
	s_nop 0
	v_pk_fma_f32 v[160:161], v[98:99], v[160:161], v[164:165] neg_lo:[0,0,1] neg_hi:[0,0,1]
	v_mul_f32_e32 v164, v140, v169
	v_fract_f32_e32 v165, v164
	v_cos_f32_e32 v164, v165
	v_sin_f32_e32 v168, v165
	v_mul_f32_e32 v165, v141, v169
	v_fract_f32_e32 v169, v165
	v_cos_f32_e32 v165, v169
	v_sin_f32_e32 v169, v169
	v_cvt_pk_bf16_f32 v156, v160, v161
	v_cvt_pk_bf16_f32 v160, v166, v167
	v_pk_mul_f32 v[164:165], v[164:165], v[130:131] op_sel_hi:[1,0]
	v_pk_mul_f32 v[168:169], v[168:169], v[130:131] op_sel_hi:[1,0]
	v_pk_mul_f32 v[170:171], v[68:69], v[164:165]
	s_nop 0
	v_pk_fma_f32 v[170:171], v[100:101], v[168:169], v[170:171]
	v_pk_mul_f32 v[168:169], v[68:69], v[168:169]
	v_cvt_pk_bf16_f32 v161, v170, v171
	v_pk_fma_f32 v[164:165], v[100:101], v[164:165], v[168:169] neg_lo:[0,0,1] neg_hi:[0,0,1]
	v_mov_b64_e32 v[168:169], s[10:11]
	v_mad_i64_i32 v[168:169], s[0:1], v172, s71, v[168:169]
	v_lshl_add_u64 v[168:169], v[168:169], 0, v[194:195]
	v_cvt_pk_bf16_f32 v157, v164, v165
	s_mov_b64 s[0:1], -1
	global_store_dwordx4 v[168:169], v[154:157], off nt
	global_store_dwordx4 v[168:169], v[158:161], off offset:128 nt
	s_cbranch_vccnz .LBB0_263
	v_cmp_gt_f32_e32 vcc, s70, v143
	s_mov_b64 s[0:1], 0
	s_nop 0
	v_cndmask_b32_e32 v143, 0, v206, vcc
	v_fma_f32 v143, -v133, v142, v143
	v_exp_f32_e32 v143, v143
	v_cndmask_b32_e32 v130, 0, v208, vcc
	v_ldexp_f32 v130, v143, v130
	v_mul_f32_e32 v130, 0x3db504f3, v130

; __device__ __forceinline__ unsigned cvt_pk_bf16(float lo, float hi) { const f32x2 v = {lo, hi}; return __builtin_bit_cast(unsigned, __builtin_convertvector(v, bf16x2_t)); }
;     __device__ __forceinline__ void operator()(g8::Acc& acc, const g8::Unit& u, int wr, int wc, int fr, int fq) const {
;     ...
;         for (int ai = 0; ai < 2; ++ai)
; #pragma unroll
;             for (int m = 0; m < 4; ++m) {
;                 const int row = row0 + ai * 128 + m * 16, pos = row & 2047, i = wr * 64 + m * 16 + fr;
;                 const float sc = isq ? exp2f(lg2 * (float)i) : exp2f(-lg2 * (float)i) * 0.08838834764831845f;
;                 const float fp = (float)pos;
;                 float o1[8], o2[8];
; #pragma unroll
;                 for (int t = 0; t < 8; ++t) {
;                     const float rev = __builtin_amdgcn_fractf(fp * fr_[t]);
;                     const float cs = __builtin_amdgcn_cosf(rev) * sc, sn = __builtin_amdgcn_sinf(rev) * sc;
;                     const float a = acc[ai][0][m][t >> 2][t & 3], b = acc[ai][1][m][t >> 2][t & 3];
;                     o1[t] = a * cs - b * sn; o2[t] = b * cs + a * sn;
;                 }
;                 bf16_t* rowp = O + (size_t)row * NPROJ + colbase;
;                 u32x4 w1, w2; w1.x = cvt_pk_bf16(o1[0], o1[1]); w1.y = cvt_pk_bf16(o1[2], o1[3]); w1.z = cvt_pk_bf16(o1[4], o1[5]); w1.w = cvt_pk_bf16(o1[6], o1[7]);
;                 w2.x = cvt_pk_bf16(o2[0], o2[1]); w2.y = cvt_pk_bf16(o2[2], o2[3]); w2.z = cvt_pk_bf16(o2[4], o2[5]); w2.w = cvt_pk_bf16(o2[6], o2[7]);
;                 *(u32x4*)rowp = w1; *(u32x4*)(rowp + 64) = w2;
.LBB0_265:
	v_add_u32_e32 v144, 0x80, v131
	v_and_b32_e32 v142, 0x7cf, v144
	v_cvt_f32_u32_e32 v167, v142
	s_and_b64 vcc, exec, s[6:7]
	v_mul_f32_e32 v142, v134, v167
	v_fract_f32_e32 v143, v142
	v_cos_f32_e32 v142, v143
	v_sin_f32_e32 v154, v143
	v_mul_f32_e32 v143, v136, v167
	v_fract_f32_e32 v155, v143
	v_cos_f32_e32 v143, v155
	v_sin_f32_e32 v155, v155
	v_pk_mul_f32 v[142:143], v[142:143], v[130:131] op_sel_hi:[1,0]
	v_pk_mul_f32 v[154:155], v[154:155], v[130:131] op_sel_hi:[1,0]
	v_pk_mul_f32 v[156:157], v[46:47], v[142:143]
	s_nop 0
	v_pk_fma_f32 v[158:159], v[62:63], v[154:155], v[156:157]
	v_pk_mul_f32 v[154:155], v[46:47], v[154:155]
	v_cvt_pk_bf16_f32 v158, v158, v159
	v_pk_fma_f32 v[142:143], v[62:63], v[142:143], v[154:155] neg_lo:[0,0,1] neg_hi:[0,0,1]
	v_mul_f32_e32 v154, v135, v167
	v_fract_f32_e32 v155, v154
	v_cos_f32_e32 v154, v155
	v_sin_f32_e32 v156, v155
	v_mul_f32_e32 v155, v137, v167
	v_fract_f32_e32 v157, v155
	v_cos_f32_e32 v155, v157
	v_sin_f32_e32 v157, v157
	v_pk_mul_f32 v[154:155], v[154:155], v[130:131] op_sel_hi:[1,0]
	v_pk_mul_f32 v[156:157], v[156:157], v[130:131] op_sel_hi:[1,0]
	v_pk_mul_f32 v[160:161], v[48:49], v[154:155]
	s_nop 0
	v_pk_fma_f32 v[160:161], v[64:65], v[156:157], v[160:161]
	v_pk_mul_f32 v[156:157], v[48:49], v[156:157]
	v_cvt_pk_bf16_f32 v159, v160, v161
	v_pk_fma_f32 v[156:157], v[64:65], v[154:155], v[156:157] neg_lo:[0,0,1] neg_hi:[0,0,1]
	v_mul_f32_e32 v154, v138, v167
	v_fract_f32_e32 v155, v154
	v_cos_f32_e32 v154, v155
	v_sin_f32_e32 v162, v155
	v_mul_f32_e32 v155, v139, v167
	v_fract_f32_e32 v163, v155
	v_cos_f32_e32 v155, v163
	v_sin_f32_e32 v163, v163
	v_pk_mul_f32 v[154:155], v[154:155], v[130:131] op_sel_hi:[1,0]
	v_pk_mul_f32 v[162:163], v[162:163], v[130:131] op_sel_hi:[1,0]
	v_pk_mul_f32 v[164:165], v[42:43], v[154:155]
	s_nop 0
	v_pk_fma_f32 v[164:165], v[58:59], v[162:163], v[164:165]
	v_pk_mul_f32 v[162:163], v[42:43], v[162:163]
	v_cvt_pk_bf16_f32 v160, v164, v165
	v_pk_fma_f32 v[162:163], v[58:59], v[154:155], v[162:163] neg_lo:[0,0,1] neg_hi:[0,0,1]
	v_mul_f32_e32 v154, v140, v167
	v_fract_f32_e32 v155, v154
	v_cos_f32_e32 v154, v155
	v_sin_f32_e32 v166, v155
	v_mul_f32_e32 v155, v141, v167
	v_fract_f32_e32 v167, v155
	v_cos_f32_e32 v155, v167
	v_sin_f32_e32 v167, v167
	v_pk_mul_f32 v[154:155], v[154:155], v[130:131] op_sel_hi:[1,0]
	v_pk_mul_f32 v[166:167], v[166:167], v[130:131] op_sel_hi:[1,0]
	v_pk_mul_f32 v[168:169], v[44:45], v[154:155]
	s_nop 0
	v_pk_fma_f32 v[168:169], v[60:61], v[166:167], v[168:169]
	v_pk_mul_f32 v[166:167], v[44:45], v[166:167]
	v_cvt_pk_bf16_f32 v161, v168, v169
	v_pk_fma_f32 v[166:167], v[60:61], v[154:155], v[166:167] neg_lo:[0,0,1] neg_hi:[0,0,1]
	v_mov_b64_e32 v[154:155], s[10:11]
	v_mad_i64_i32 v[154:155], s[0:1], v144, s71, v[154:155]
	v_lshl_add_u64 v[170:171], v[154:155], 0, v[194:195]
	v_cvt_pk_bf16_f32 v154, v142, v143
	v_cvt_pk_bf16_f32 v155, v156, v157
	v_cvt_pk_bf16_f32 v156, v162, v163
	v_cvt_pk_bf16_f32 v157, v166, v167
	s_mov_b64 s[0:1], -1
	global_store_dwordx4 v[170:171], v[154:157], off nt
	global_store_dwordx4 v[170:171], v[158:161], off offset:128 nt
	s_cbranch_vccnz .LBB0_267
	v_cmp_gt_f32_e32 vcc, s70, v148
	s_mov_b64 s[0:1], 0
	s_nop 0
	v_cndmask_b32_e32 v142, 0, v206, vcc
	v_fma_f32 v142, -v133, v146, v142
	v_exp_f32_e32 v142, v142
	v_cndmask_b32_e32 v130, 0, v208, vcc
	v_ldexp_f32 v130, v142, v130
	v_mul_f32_e32 v130, 0x3db504f3, v130

; __device__ __forceinline__ unsigned cvt_pk_bf16(float lo, float hi) { const f32x2 v = {lo, hi}; return __builtin_bit_cast(unsigned, __builtin_convertvector(v, bf16x2_t)); }
;     __device__ __forceinline__ void operator()(g8::Acc& acc, const g8::Unit& u, int wr, int wc, int fr, int fq) const {
;     ...
;         for (int ai = 0; ai < 2; ++ai)
; #pragma unroll
;             for (int m = 0; m < 4; ++m) {
;                 const int row = row0 + ai * 128 + m * 16, pos = row & 2047, i = wr * 64 + m * 16 + fr;
;                 const float sc = isq ? exp2f(lg2 * (float)i) : exp2f(-lg2 * (float)i) * 0.08838834764831845f;
;                 const float fp = (float)pos;
;                 float o1[8], o2[8];
; #pragma unroll
;                 for (int t = 0; t < 8; ++t) {
;                     const float rev = __builtin_amdgcn_fractf(fp * fr_[t]);
;                     const float cs = __builtin_amdgcn_cosf(rev) * sc, sn = __builtin_amdgcn_sinf(rev) * sc;
;                     const float a = acc[ai][0][m][t >> 2][t & 3], b = acc[ai][1][m][t >> 2][t & 3];
;                     o1[t] = a * cs - b * sn; o2[t] = b * cs + a * sn;
;                 }
;                 bf16_t* rowp = O + (size_t)row * NPROJ + colbase;
;                 u32x4 w1, w2; w1.x = cvt_pk_bf16(o1[0], o1[1]); w1.y = cvt_pk_bf16(o1[2], o1[3]); w1.z = cvt_pk_bf16(o1[4], o1[5]); w1.w = cvt_pk_bf16(o1[6], o1[7]);
;                 w2.x = cvt_pk_bf16(o2[0], o2[1]); w2.y = cvt_pk_bf16(o2[2], o2[3]); w2.z = cvt_pk_bf16(o2[4], o2[5]); w2.w = cvt_pk_bf16(o2[6], o2[7]);
;                 *(u32x4*)rowp = w1; *(u32x4*)(rowp + 64) = w2;
.LBB0_269:
	v_add_u32_e32 v144, 0x90, v131
	v_and_b32_e32 v142, 0x7df, v144
	v_cvt_f32_u32_e32 v146, v142
	s_and_b64 vcc, exec, s[6:7]
	v_mul_f32_e32 v142, v134, v146
	v_fract_f32_e32 v143, v142
	v_cos_f32_e32 v142, v143
	v_sin_f32_e32 v148, v143
	v_mul_f32_e32 v143, v136, v146
	v_fract_f32_e32 v149, v143
	v_cos_f32_e32 v143, v149
	v_sin_f32_e32 v149, v149
	v_pk_mul_f32 v[142:143], v[142:143], v[130:131] op_sel_hi:[1,0]
	v_pk_mul_f32 v[148:149], v[148:149], v[130:131] op_sel_hi:[1,0]
	v_pk_mul_f32 v[154:155], v[30:31], v[142:143]
	s_nop 0
	v_pk_fma_f32 v[158:159], v[54:55], v[148:149], v[154:155]
	v_pk_mul_f32 v[148:149], v[30:31], v[148:149]
	v_cvt_pk_bf16_f32 v158, v158, v159
	v_pk_fma_f32 v[142:143], v[54:55], v[142:143], v[148:149] neg_lo:[0,0,1] neg_hi:[0,0,1]
	v_mul_f32_e32 v148, v135, v146
	v_fract_f32_e32 v149, v148
	v_cos_f32_e32 v148, v149
	v_sin_f32_e32 v154, v149
	v_mul_f32_e32 v149, v137, v146
	v_fract_f32_e32 v155, v149
	v_cos_f32_e32 v149, v155
	v_sin_f32_e32 v155, v155
	v_pk_mul_f32 v[148:149], v[148:149], v[130:131] op_sel_hi:[1,0]
	v_pk_mul_f32 v[154:155], v[154:155], v[130:131] op_sel_hi:[1,0]
	v_pk_mul_f32 v[156:157], v[32:33], v[148:149]
	s_nop 0
	v_pk_fma_f32 v[160:161], v[56:57], v[154:155], v[156:157]
	v_pk_mul_f32 v[154:155], v[32:33], v[154:155]
	v_cvt_pk_bf16_f32 v159, v160, v161
	v_pk_fma_f32 v[148:149], v[56:57], v[148:149], v[154:155] neg_lo:[0,0,1] neg_hi:[0,0,1]
	v_mul_f32_e32 v154, v138, v146
	v_fract_f32_e32 v155, v154
	v_cos_f32_e32 v154, v155
	v_sin_f32_e32 v156, v155
	v_mul_f32_e32 v155, v139, v146
	v_fract_f32_e32 v157, v155
	v_cos_f32_e32 v155, v157
	v_sin_f32_e32 v157, v157
	v_pk_mul_f32 v[154:155], v[154:155], v[130:131] op_sel_hi:[1,0]
	v_pk_mul_f32 v[156:157], v[156:157], v[130:131] op_sel_hi:[1,0]
	v_pk_mul_f32 v[162:163], v[26:27], v[154:155]
	s_nop 0
	v_pk_fma_f32 v[162:163], v[50:51], v[156:157], v[162:163]
	v_pk_mul_f32 v[156:157], v[26:27], v[156:157]
	v_cvt_pk_bf16_f32 v160, v162, v163
	v_pk_fma_f32 v[156:157], v[50:51], v[154:155], v[156:157] neg_lo:[0,0,1] neg_hi:[0,0,1]
	v_mul_f32_e32 v154, v140, v146
	v_mul_f32_e32 v146, v141, v146
	v_fract_f32_e32 v155, v154
	v_fract_f32_e32 v146, v146
	v_cos_f32_e32 v154, v155
	v_sin_f32_e32 v164, v155
	v_cos_f32_e32 v155, v146
	v_sin_f32_e32 v165, v146
	v_cvt_pk_bf16_f32 v156, v156, v157
	v_pk_mul_f32 v[154:155], v[154:155], v[130:131] op_sel_hi:[1,0]
	v_pk_mul_f32 v[164:165], v[164:165], v[130:131] op_sel_hi:[1,0]
	v_pk_mul_f32 v[166:167], v[28:29], v[154:155]
	s_nop 0
	v_pk_fma_f32 v[166:167], v[52:53], v[164:165], v[166:167]
	v_pk_mul_f32 v[164:165], v[28:29], v[164:165]
	v_cvt_pk_bf16_f32 v161, v166, v167
	v_pk_fma_f32 v[164:165], v[52:53], v[154:155], v[164:165] neg_lo:[0,0,1] neg_hi:[0,0,1]
	v_mov_b64_e32 v[154:155], s[10:11]
	v_mad_i64_i32 v[154:155], s[0:1], v144, s71, v[154:155]
	v_lshl_add_u64 v[168:169], v[154:155], 0, v[194:195]
	v_cvt_pk_bf16_f32 v154, v142, v143
	v_cvt_pk_bf16_f32 v155, v148, v149
	v_cvt_pk_bf16_f32 v157, v164, v165
	s_mov_b64 s[0:1], -1
	global_store_dwordx4 v[168:169], v[154:157], off nt
	global_store_dwordx4 v[168:169], v[158:161], off offset:128 nt
	s_cbranch_vccnz .LBB0_271
	v_cmp_gt_f32_e32 vcc, s70, v150
	s_mov_b64 s[0:1], 0
	s_nop 0
	v_cndmask_b32_e32 v142, 0, v206, vcc
	v_fma_f32 v142, -v133, v147, v142
	v_exp_f32_e32 v142, v142
	v_cndmask_b32_e32 v130, 0, v208, vcc
	v_ldexp_f32 v130, v142, v130
	v_mul_f32_e32 v130, 0x3db504f3, v130

; __device__ __forceinline__ unsigned cvt_pk_bf16(float lo, float hi) { const f32x2 v = {lo, hi}; return __builtin_bit_cast(unsigned, __builtin_convertvector(v, bf16x2_t)); }
;     __device__ __forceinline__ void operator()(g8::Acc& acc, const g8::Unit& u, int wr, int wc, int fr, int fq) const {
;     ...
;         for (int ai = 0; ai < 2; ++ai)
; #pragma unroll
;             for (int m = 0; m < 4; ++m) {
;                 const int row = row0 + ai * 128 + m * 16, pos = row & 2047, i = wr * 64 + m * 16 + fr;
;                 const float sc = isq ? exp2f(lg2 * (float)i) : exp2f(-lg2 * (float)i) * 0.08838834764831845f;
;                 const float fp = (float)pos;
;                 float o1[8], o2[8];
; #pragma unroll
;                 for (int t = 0; t < 8; ++t) {
;                     const float rev = __builtin_amdgcn_fractf(fp * fr_[t]);
;                     const float cs = __builtin_amdgcn_cosf(rev) * sc, sn = __builtin_amdgcn_sinf(rev) * sc;
;                     const float a = acc[ai][0][m][t >> 2][t & 3], b = acc[ai][1][m][t >> 2][t & 3];
;                     o1[t] = a * cs - b * sn; o2[t] = b * cs + a * sn;
;                 }
;                 bf16_t* rowp = O + (size_t)row * NPROJ + colbase;
;                 u32x4 w1, w2; w1.x = cvt_pk_bf16(o1[0], o1[1]); w1.y = cvt_pk_bf16(o1[2], o1[3]); w1.z = cvt_pk_bf16(o1[4], o1[5]); w1.w = cvt_pk_bf16(o1[6], o1[7]);
;                 w2.x = cvt_pk_bf16(o2[0], o2[1]); w2.y = cvt_pk_bf16(o2[2], o2[3]); w2.z = cvt_pk_bf16(o2[4], o2[5]); w2.w = cvt_pk_bf16(o2[6], o2[7]);
;                 *(u32x4*)rowp = w1; *(u32x4*)(rowp + 64) = w2;
.LBB0_273:
	v_add_u32_e32 v144, 0xa0, v131
	v_and_b32_e32 v142, 0x7ef, v144
	v_cvt_f32_u32_e32 v161, v142
	s_and_b64 vcc, exec, s[6:7]
	v_mul_f32_e32 v142, v134, v161
	v_fract_f32_e32 v143, v142
	v_cos_f32_e32 v142, v143
	v_sin_f32_e32 v146, v143
	v_mul_f32_e32 v143, v136, v161
	v_fract_f32_e32 v147, v143
	v_cos_f32_e32 v143, v147
	v_sin_f32_e32 v147, v147
	v_pk_mul_f32 v[142:143], v[142:143], v[130:131] op_sel_hi:[1,0]
	v_pk_mul_f32 v[146:147], v[146:147], v[130:131] op_sel_hi:[1,0]
	v_pk_mul_f32 v[148:149], v[14:15], v[142:143]
	s_nop 0
	v_pk_fma_f32 v[150:151], v[38:39], v[146:147], v[148:149]
	v_pk_mul_f32 v[146:147], v[14:15], v[146:147]
	s_nop 0
	v_pk_fma_f32 v[142:143], v[38:39], v[142:143], v[146:147] neg_lo:[0,0,1] neg_hi:[0,0,1]
	v_mul_f32_e32 v146, v135, v161
	v_fract_f32_e32 v147, v146
	v_cos_f32_e32 v146, v147
	v_sin_f32_e32 v148, v147
	v_mul_f32_e32 v147, v137, v161
	v_fract_f32_e32 v149, v147
	v_cos_f32_e32 v147, v149
	v_sin_f32_e32 v149, v149
	v_pk_mul_f32 v[146:147], v[146:147], v[130:131] op_sel_hi:[1,0]
	v_pk_mul_f32 v[148:149], v[148:149], v[130:131] op_sel_hi:[1,0]
	v_pk_mul_f32 v[154:155], v[16:17], v[146:147]
	s_nop 0
	v_pk_fma_f32 v[156:157], v[40:41], v[148:149], v[154:155]
	v_pk_mul_f32 v[148:149], v[16:17], v[148:149]
	s_nop 0
	v_pk_fma_f32 v[148:149], v[40:41], v[146:147], v[148:149] neg_lo:[0,0,1] neg_hi:[0,0,1]
	v_mul_f32_e32 v146, v138, v161
	v_fract_f32_e32 v147, v146
	v_cos_f32_e32 v146, v147
	v_sin_f32_e32 v154, v147
	v_mul_f32_e32 v147, v139, v161
	v_fract_f32_e32 v155, v147
	v_cos_f32_e32 v147, v155
	v_sin_f32_e32 v155, v155
	v_pk_mul_f32 v[146:147], v[146:147], v[130:131] op_sel_hi:[1,0]
	v_pk_mul_f32 v[154:155], v[154:155], v[130:131] op_sel_hi:[1,0]
	v_pk_mul_f32 v[158:159], v[10:11], v[146:147]
	s_nop 0
	v_pk_fma_f32 v[158:159], v[34:35], v[154:155], v[158:159]
	v_pk_mul_f32 v[154:155], v[10:11], v[154:155]
	s_nop 0
	v_pk_fma_f32 v[154:155], v[34:35], v[146:147], v[154:155] neg_lo:[0,0,1] neg_hi:[0,0,1]
	v_mul_f32_e32 v146, v140, v161
	v_fract_f32_e32 v147, v146
	v_cos_f32_e32 v146, v147
	v_sin_f32_e32 v160, v147
	v_mul_f32_e32 v147, v141, v161
	v_fract_f32_e32 v161, v147
	v_cos_f32_e32 v147, v161
	v_sin_f32_e32 v161, v161
	v_pk_mul_f32 v[146:147], v[146:147], v[130:131] op_sel_hi:[1,0]
	v_pk_mul_f32 v[160:161], v[160:161], v[130:131] op_sel_hi:[1,0]
	v_pk_mul_f32 v[162:163], v[12:13], v[146:147]
	s_nop 0
	v_pk_fma_f32 v[162:163], v[36:37], v[160:161], v[162:163]
	v_pk_mul_f32 v[160:161], v[12:13], v[160:161]
	s_nop 0
	v_pk_fma_f32 v[160:161], v[36:37], v[146:147], v[160:161] neg_lo:[0,0,1] neg_hi:[0,0,1]
	v_mov_b64_e32 v[146:147], s[10:11]
	v_mad_i64_i32 v[146:147], s[0:1], v144, s71, v[146:147]
	v_lshl_add_u64 v[164:165], v[146:147], 0, v[194:195]
	v_cvt_pk_bf16_f32 v146, v142, v143
	v_cvt_pk_bf16_f32 v147, v148, v149
	v_cvt_pk_bf16_f32 v148, v154, v155
	v_cvt_pk_bf16_f32 v149, v160, v161
	s_mov_b64 s[0:1], -1
	v_cvt_pk_bf16_f32 v154, v150, v151
	v_cvt_pk_bf16_f32 v155, v156, v157
	v_cvt_pk_bf16_f32 v156, v158, v159
	v_cvt_pk_bf16_f32 v157, v162, v163
	global_store_dwordx4 v[164:165], v[146:149], off nt
	global_store_dwordx4 v[164:165], v[154:157], off offset:128 nt
	s_cbranch_vccnz .LBB0_275
	v_cmp_gt_f32_e32 vcc, s70, v152
	s_mov_b64 s[0:1], 0
	s_nop 0
	v_cndmask_b32_e32 v142, 0, v206, vcc
	v_fma_f32 v142, -v133, v145, v142
	v_exp_f32_e32 v142, v142
	v_cndmask_b32_e32 v130, 0, v208, vcc
	v_ldexp_f32 v130, v142, v130
	v_mul_f32_e32 v130, 0x3db504f3, v130

; __device__ __forceinline__ unsigned cvt_pk_bf16(float lo, float hi) { const f32x2 v = {lo, hi}; return __builtin_bit_cast(unsigned, __builtin_convertvector(v, bf16x2_t)); }
;     __device__ __forceinline__ void operator()(g8::Acc& acc, const g8::Unit& u, int wr, int wc, int fr, int fq) const {
;     ...
;         for (int ai = 0; ai < 2; ++ai)
; #pragma unroll
;             for (int m = 0; m < 4; ++m) {
;                 const int row = row0 + ai * 128 + m * 16, pos = row & 2047, i = wr * 64 + m * 16 + fr;
;                 const float sc = isq ? exp2f(lg2 * (float)i) : exp2f(-lg2 * (float)i) * 0.08838834764831845f;
;                 const float fp = (float)pos;
;                 float o1[8], o2[8];
; #pragma unroll
;                 for (int t = 0; t < 8; ++t) {
;                     const float rev = __builtin_amdgcn_fractf(fp * fr_[t]);
;                     const float cs = __builtin_amdgcn_cosf(rev) * sc, sn = __builtin_amdgcn_sinf(rev) * sc;
;                     const float a = acc[ai][0][m][t >> 2][t & 3], b = acc[ai][1][m][t >> 2][t & 3];
;                     o1[t] = a * cs - b * sn; o2[t] = b * cs + a * sn;
;                 }
;                 bf16_t* rowp = O + (size_t)row * NPROJ + colbase;
;                 u32x4 w1, w2; w1.x = cvt_pk_bf16(o1[0], o1[1]); w1.y = cvt_pk_bf16(o1[2], o1[3]); w1.z = cvt_pk_bf16(o1[4], o1[5]); w1.w = cvt_pk_bf16(o1[6], o1[7]);
;                 w2.x = cvt_pk_bf16(o2[0], o2[1]); w2.y = cvt_pk_bf16(o2[2], o2[3]); w2.z = cvt_pk_bf16(o2[4], o2[5]); w2.w = cvt_pk_bf16(o2[6], o2[7]);
;                 *(u32x4*)rowp = w1; *(u32x4*)(rowp + 64) = w2;
.LBB0_277:
	v_add_u32_e32 v133, 0xb0, v131
	v_and_b32_e32 v142, 0x7ff, v133
	v_cvt_f32_u32_e32 v150, v142
	v_mul_f32_e32 v134, v134, v150
	v_fract_f32_e32 v134, v134
	v_cos_f32_e32 v142, v134
	v_sin_f32_e32 v144, v134
	v_mul_f32_e32 v134, v136, v150
	v_fract_f32_e32 v134, v134
	v_cos_f32_e32 v143, v134
	v_sin_f32_e32 v145, v134
	v_mul_f32_e32 v134, v135, v150
	v_fract_f32_e32 v135, v134
	v_cos_f32_e32 v134, v135
	v_sin_f32_e32 v136, v135
	v_mul_f32_e32 v135, v137, v150
	v_fract_f32_e32 v137, v135
	v_cos_f32_e32 v135, v137
	v_sin_f32_e32 v137, v137
	v_pk_mul_f32 v[142:143], v[142:143], v[130:131] op_sel_hi:[1,0]
	v_pk_mul_f32 v[144:145], v[144:145], v[130:131] op_sel_hi:[1,0]
	v_pk_mul_f32 v[146:147], v[6:7], v[142:143]
	v_pk_mul_f32 v[134:135], v[134:135], v[130:131] op_sel_hi:[1,0]
	v_pk_fma_f32 v[146:147], v[22:23], v[144:145], v[146:147]
	v_pk_mul_f32 v[144:145], v[6:7], v[144:145]
	v_pk_mul_f32 v[136:137], v[136:137], v[130:131] op_sel_hi:[1,0]
	v_pk_fma_f32 v[142:143], v[22:23], v[142:143], v[144:145] neg_lo:[0,0,1] neg_hi:[0,0,1]
	v_pk_mul_f32 v[144:145], v[8:9], v[134:135]
	s_nop 0
	v_pk_fma_f32 v[144:145], v[24:25], v[136:137], v[144:145]
	v_pk_mul_f32 v[136:137], v[8:9], v[136:137]
	s_nop 0
	v_pk_fma_f32 v[136:137], v[24:25], v[134:135], v[136:137] neg_lo:[0,0,1] neg_hi:[0,0,1]
	v_mul_f32_e32 v134, v138, v150
	v_fract_f32_e32 v135, v134
	v_cos_f32_e32 v134, v135
	v_sin_f32_e32 v138, v135
	v_mul_f32_e32 v135, v139, v150
	v_fract_f32_e32 v139, v135
	v_cos_f32_e32 v135, v139
	v_sin_f32_e32 v139, v139
	v_pk_mul_f32 v[134:135], v[134:135], v[130:131] op_sel_hi:[1,0]
	v_pk_mul_f32 v[138:139], v[138:139], v[130:131] op_sel_hi:[1,0]
	v_pk_mul_f32 v[148:149], v[2:3], v[134:135]
	s_nop 0
	v_pk_fma_f32 v[148:149], v[18:19], v[138:139], v[148:149]
	v_pk_mul_f32 v[138:139], v[2:3], v[138:139]
	s_nop 0
	v_pk_fma_f32 v[138:139], v[18:19], v[134:135], v[138:139] neg_lo:[0,0,1] neg_hi:[0,0,1]
	v_mul_f32_e32 v134, v140, v150
	v_fract_f32_e32 v135, v134
	v_cos_f32_e32 v134, v135
	v_sin_f32_e32 v140, v135
	v_mul_f32_e32 v135, v141, v150
	v_fract_f32_e32 v141, v135
	v_cos_f32_e32 v135, v141
	v_sin_f32_e32 v141, v141
	v_pk_mul_f32 v[134:135], v[134:135], v[130:131] op_sel_hi:[1,0]
	v_pk_mul_f32 v[140:141], v[140:141], v[130:131] op_sel_hi:[1,0]
	v_pk_mul_f32 v[150:151], v[4:5], v[134:135]
	s_nop 0
	v_pk_fma_f32 v[150:151], v[20:21], v[140:141], v[150:151]
	v_pk_mul_f32 v[140:141], v[4:5], v[140:141]
	s_nop 0
	v_pk_fma_f32 v[140:141], v[20:21], v[134:135], v[140:141] neg_lo:[0,0,1] neg_hi:[0,0,1]
	v_mov_b64_e32 v[134:135], s[10:11]
	v_mad_i64_i32 v[134:135], s[0:1], v133, s71, v[134:135]
	v_lshl_add_u64 v[152:153], v[134:135], 0, v[194:195]
	v_cvt_pk_bf16_f32 v134, v142, v143
	v_cvt_pk_bf16_f32 v135, v136, v137
	v_cvt_pk_bf16_f32 v136, v138, v139
	v_cvt_pk_bf16_f32 v137, v140, v141
	v_cvt_pk_bf16_f32 v138, v146, v147
	v_cvt_pk_bf16_f32 v139, v144, v145
	v_cvt_pk_bf16_f32 v140, v148, v149
	v_cvt_pk_bf16_f32 v141, v150, v151
	global_store_dwordx4 v[152:153], v[134:137], off nt
	global_store_dwordx4 v[152:153], v[138:141], off offset:128 nt
	s_mov_b64 s[0:1], 0
; __device__ __forceinline__ unsigned cvt_pk_bf16(float lo, float hi) { const f32x2 v = {lo, hi}; return __builtin_bit_cast(unsigned, __builtin_convertvector(v, bf16x2_t)); }
;     __device__ __forceinline__ void operator()(g8::Acc& acc, const g8::Unit& u, int wr, int wc, int fr, int fq) const {
;     ...
;         if (pn >= 12) {
;             const int col0 = pn * 256 + wc * 32 + 8 * fq;
; #pragma unroll
;             for (int ai = 0; ai < 2; ++ai)
; #pragma unroll
;                 for (int m = 0; m < 4; ++m) { bf16_t* rowp = O + (size_t)(row0 + ai * 128 + m * 16) * NPROJ + col0;
; #pragma unroll
;                     for (int bj = 0; bj < 2; ++bj) { const f32x4 v0 = acc[ai][bj][m][0], v1 = acc[ai][bj][m][1];
;                         u32x4 w; w.x = cvt_pk_bf16(v0[0], v0[1]); w.y = cvt_pk_bf16(v0[2], v0[3]); w.z = cvt_pk_bf16(v1[0], v1[1]); w.w = cvt_pk_bf16(v1[2], v1[3]);
;                         *(u32x4*)(rowp + bj * 128) = w; } }
;             return;
.LBB0_278:
	s_and_b64 vcc, exec, s[0:1]
	s_cbranch_vccz .LBB0_280
	s_lshl_b32 s0, s44, 8
	s_or_b32 s0, s0, s87
	v_lshl_add_u32 v194, v132, 3, s0
	v_mov_b64_e32 v[138:139], s[10:11]
	v_mad_i64_i32 v[134:135], s[0:1], v131, s71, v[138:139]
	v_lshlrev_b64 v[140:141], 1, v[194:195]
	v_lshl_add_u64 v[142:143], v[134:135], 0, v[140:141]
	v_cvt_pk_bf16_f32 v134, v126, v127
	v_cvt_pk_bf16_f32 v135, v128, v129
	v_cvt_pk_bf16_f32 v136, v122, v123
	v_cvt_pk_bf16_f32 v137, v124, v125
	global_store_dwordx4 v[142:143], v[134:137], off nt
	v_or_b32_e32 v130, 16, v131
	s_nop 0
	v_cvt_pk_bf16_f32 v134, v94, v95
	v_cvt_pk_bf16_f32 v135, v96, v97
	v_cvt_pk_bf16_f32 v136, v90, v91
	v_cvt_pk_bf16_f32 v137, v92, v93
	global_store_dwordx4 v[142:143], v[134:137], off offset:256 nt
	s_nop 1
	v_mad_i64_i32 v[134:135], s[0:1], v130, s71, v[138:139]
	v_lshl_add_u64 v[142:143], v[134:135], 0, v[140:141]
	v_cvt_pk_bf16_f32 v134, v118, v119
	v_cvt_pk_bf16_f32 v135, v120, v121
	v_cvt_pk_bf16_f32 v136, v114, v115
	v_cvt_pk_bf16_f32 v137, v116, v117
	global_store_dwordx4 v[142:143], v[134:137], off nt
	v_or_b32_e32 v130, 32, v131
	s_nop 0
	v_cvt_pk_bf16_f32 v134, v86, v87
	v_cvt_pk_bf16_f32 v135, v88, v89
	v_cvt_pk_bf16_f32 v136, v82, v83
	v_cvt_pk_bf16_f32 v137, v84, v85
	global_store_dwordx4 v[142:143], v[134:137], off offset:256 nt
	s_nop 1
	v_mad_i64_i32 v[134:135], s[0:1], v130, s71, v[138:139]
	v_lshl_add_u64 v[142:143], v[134:135], 0, v[140:141]
	v_cvt_pk_bf16_f32 v134, v110, v111
	v_cvt_pk_bf16_f32 v135, v112, v113
	v_cvt_pk_bf16_f32 v136, v106, v107
	v_cvt_pk_bf16_f32 v137, v108, v109
	global_store_dwordx4 v[142:143], v[134:137], off nt
	v_or_b32_e32 v130, 48, v131
	s_nop 0
	v_cvt_pk_bf16_f32 v134, v78, v79
	v_cvt_pk_bf16_f32 v135, v80, v81
	v_cvt_pk_bf16_f32 v136, v74, v75
	v_cvt_pk_bf16_f32 v137, v76, v77
	global_store_dwordx4 v[142:143], v[134:137], off offset:256 nt
	s_nop 1
	v_mad_i64_i32 v[134:135], s[0:1], v130, s71, v[138:139]
	v_lshl_add_u64 v[142:143], v[134:135], 0, v[140:141]
	v_cvt_pk_bf16_f32 v134, v102, v103
	v_cvt_pk_bf16_f32 v135, v104, v105
	v_cvt_pk_bf16_f32 v136, v98, v99
	v_cvt_pk_bf16_f32 v137, v100, v101
	global_store_dwordx4 v[142:143], v[134:137], off nt
	v_add_u32_e32 v130, 0x80, v131
	s_nop 0
	v_cvt_pk_bf16_f32 v134, v70, v71
	v_cvt_pk_bf16_f32 v135, v72, v73
	v_cvt_pk_bf16_f32 v136, v66, v67
	v_cvt_pk_bf16_f32 v137, v68, v69
	global_store_dwordx4 v[142:143], v[134:137], off offset:256 nt
	s_nop 1
	v_mad_i64_i32 v[134:135], s[0:1], v130, s71, v[138:139]
	v_lshl_add_u64 v[142:143], v[134:135], 0, v[140:141]
	v_cvt_pk_bf16_f32 v134, v62, v63
	v_cvt_pk_bf16_f32 v135, v64, v65
	v_cvt_pk_bf16_f32 v136, v58, v59
	v_cvt_pk_bf16_f32 v137, v60, v61
	global_store_dwordx4 v[142:143], v[134:137], off nt
	v_add_u32_e32 v130, 0x90, v131
	s_nop 0
	v_cvt_pk_bf16_f32 v134, v46, v47
	v_cvt_pk_bf16_f32 v135, v48, v49
	v_cvt_pk_bf16_f32 v136, v42, v43
	v_cvt_pk_bf16_f32 v137, v44, v45
	global_store_dwordx4 v[142:143], v[134:137], off offset:256 nt
	s_nop 1
	v_mad_i64_i32 v[134:135], s[0:1], v130, s71, v[138:139]
	v_lshl_add_u64 v[142:143], v[134:135], 0, v[140:141]
	v_cvt_pk_bf16_f32 v134, v54, v55
	v_cvt_pk_bf16_f32 v135, v56, v57
	v_cvt_pk_bf16_f32 v136, v50, v51
	v_cvt_pk_bf16_f32 v137, v52, v53
	global_store_dwordx4 v[142:143], v[134:137], off nt
	v_add_u32_e32 v130, 0xa0, v131
	s_nop 0
	v_cvt_pk_bf16_f32 v134, v30, v31
	v_cvt_pk_bf16_f32 v135, v32, v33
	v_cvt_pk_bf16_f32 v136, v26, v27
	v_cvt_pk_bf16_f32 v137, v28, v29
	global_store_dwordx4 v[142:143], v[134:137], off offset:256 nt
	s_nop 1
	v_mad_i64_i32 v[134:135], s[0:1], v130, s71, v[138:139]
	v_lshl_add_u64 v[142:143], v[134:135], 0, v[140:141]
	v_cvt_pk_bf16_f32 v134, v38, v39
	v_cvt_pk_bf16_f32 v135, v40, v41
	v_cvt_pk_bf16_f32 v136, v34, v35
	v_cvt_pk_bf16_f32 v137, v36, v37
	global_store_dwordx4 v[142:143], v[134:137], off nt
	v_add_u32_e32 v130, 0xb0, v131
	s_nop 0
	v_cvt_pk_bf16_f32 v134, v14, v15
	v_cvt_pk_bf16_f32 v135, v16, v17
	v_cvt_pk_bf16_f32 v136, v10, v11
	v_cvt_pk_bf16_f32 v137, v12, v13
	global_store_dwordx4 v[142:143], v[134:137], off offset:256 nt
	s_nop 1
	v_mad_i64_i32 v[134:135], s[0:1], v130, s71, v[138:139]
	v_lshl_add_u64 v[138:139], v[134:135], 0, v[140:141]
	v_cvt_pk_bf16_f32 v134, v22, v23
	v_cvt_pk_bf16_f32 v135, v24, v25
	v_cvt_pk_bf16_f32 v136, v18, v19
	v_cvt_pk_bf16_f32 v137, v20, v21
	global_store_dwordx4 v[138:139], v[134:137], off nt
	s_nop 1
	v_cvt_pk_bf16_f32 v134, v6, v7
	v_cvt_pk_bf16_f32 v135, v8, v9
	v_cvt_pk_bf16_f32 v136, v2, v3
	v_cvt_pk_bf16_f32 v137, v4, v5
	global_store_dwordx4 v[138:139], v[134:137], off offset:256 nt

; __device__ __forceinline__ unsigned cvt_pk_bf16(float lo, float hi) { const f32x2 v = {lo, hi}; return __builtin_bit_cast(unsigned, __builtin_convertvector(v, bf16x2_t)); }
;     __device__ __forceinline__ void operator()(g8::Acc& acc, const g8::Unit& u, int wr, int wc, int fr, int fq) const {
;     ...
;         if (pn < 4) {
;             const int col0 = pn * 256 + wc * 32 + 8 * fq;
; #pragma unroll
;             for (int ai = 0; ai < 2; ++ai)
; #pragma unroll
;                 for (int m = 0; m < 4; ++m) { const int row = row0 + ai * 128 + m * 16;
; #pragma unroll
;                     for (int bj = 0; bj < 2; ++bj) { const f32x4 v0 = acc[ai][bj][m][0], v1 = acc[ai][bj][m][1]; const int col = col0 + bj * 128;
;                         u32x4 w; w.x = cvt_pk_bf16(v0[0], v0[1]); w.y = cvt_pk_bf16(v0[2], v0[3]); w.z = cvt_pk_bf16(v1[0], v1[1]); w.w = cvt_pk_bf16(v1[2], v1[3]);
;                         *(u32x4*)(U2 + ((size_t)((row >> 11) * 64 + (col >> 4)) * 2048 + (row & 2047)) * 16 + (col & 15)) = w; } }
;             return;
.LBB0_281:
	s_andn2_b64 vcc, exec, s[0:1]
	s_cbranch_vccnz .LBB0_229
	s_lshl_b32 s0, s44, 8
	s_or_b32 s0, s0, s87
	v_lshl_add_u32 v130, v132, 3, s0
	s_ashr_i32 s0, s73, 5
	s_andn2_b32 s0, s0, 63
	v_ashrrev_i32_e32 v133, 4, v130
	v_cvt_pk_bf16_f32 v126, v126, v127
	v_cvt_pk_bf16_f32 v127, v128, v129
	v_cvt_pk_bf16_f32 v128, v122, v123
	v_add_u32_e32 v122, s0, v133
	v_ashrrev_i32_e32 v123, 31, v122
	v_cvt_pk_bf16_f32 v129, v124, v125
	v_lshlrev_b64 v[122:123], 16, v[122:123]
	v_lshlrev_b32_e32 v124, 5, v131
	v_lshl_add_u64 v[122:123], s[12:13], 0, v[122:123]
	v_and_b32_e32 v194, 0xf9e0, v124
	v_lshlrev_b32_e32 v124, 4, v132
	v_lshl_add_u64 v[122:123], v[122:123], 0, v[194:195]
	v_and_b32_e32 v124, 16, v124
	v_mov_b32_e32 v125, v195
	v_lshl_add_u64 v[122:123], v[122:123], 0, v[124:125]
	global_store_dwordx4 v[122:123], v[126:129], off nt
	v_cvt_pk_bf16_f32 v70, v70, v71
	v_cvt_pk_bf16_f32 v71, v72, v73
	v_add_u32_e32 v126, 0x80, v130
	v_cvt_pk_bf16_f32 v72, v66, v67
	v_add_u32_e32 v66, 0x80, v131
	v_ashrrev_i32_e32 v128, 4, v126
	v_ashrrev_i32_e32 v67, 5, v66
	v_cvt_pk_bf16_f32 v94, v94, v95
	v_cvt_pk_bf16_f32 v95, v96, v97
	v_cvt_pk_bf16_f32 v96, v90, v91
	v_add_u32_e32 v90, s0, v128
	v_and_b32_e32 v67, 0xffffffc0, v67
	v_ashrrev_i32_e32 v91, 31, v90
	v_cvt_pk_bf16_f32 v62, v62, v63
	v_cvt_pk_bf16_f32 v63, v64, v65
	v_cvt_pk_bf16_f32 v64, v58, v59
	v_add_u32_e32 v58, v67, v133
	v_cvt_pk_bf16_f32 v46, v46, v47
	v_cvt_pk_bf16_f32 v47, v48, v49
	v_cvt_pk_bf16_f32 v48, v42, v43
	v_add_u32_e32 v42, v128, v67
	v_lshlrev_b64 v[90:91], 16, v[90:91]
	v_ashrrev_i32_e32 v59, 31, v58
	v_ashrrev_i32_e32 v43, 31, v42
	v_lshl_add_u64 v[90:91], s[12:13], 0, v[90:91]
	v_cvt_pk_bf16_f32 v65, v60, v61
	v_lshlrev_b64 v[58:59], 16, v[58:59]
	v_lshlrev_b32_e32 v60, 5, v66
	v_lshlrev_b64 v[42:43], 16, v[42:43]
	v_lshl_add_u64 v[90:91], v[90:91], 0, v[194:195]
	v_lshl_add_u64 v[58:59], s[12:13], 0, v[58:59]
	v_and_b32_e32 v194, 0xf9e0, v60
	v_lshl_add_u64 v[42:43], s[12:13], 0, v[42:43]
	v_lshl_add_u64 v[58:59], v[58:59], 0, v[194:195]
	v_lshl_add_u64 v[42:43], v[42:43], 0, v[194:195]
	v_cvt_pk_bf16_f32 v97, v92, v93
	v_lshl_add_u64 v[126:127], v[90:91], 0, v[124:125]
	v_cvt_pk_bf16_f32 v90, v118, v119
	v_cvt_pk_bf16_f32 v91, v120, v121
	v_cvt_pk_bf16_f32 v92, v114, v115
	v_cvt_pk_bf16_f32 v93, v116, v117
	v_cvt_pk_bf16_f32 v86, v86, v87
	v_cvt_pk_bf16_f32 v87, v88, v89
	v_cvt_pk_bf16_f32 v88, v82, v83
	v_cvt_pk_bf16_f32 v89, v84, v85
	v_cvt_pk_bf16_f32 v82, v110, v111
	v_cvt_pk_bf16_f32 v83, v112, v113
	v_cvt_pk_bf16_f32 v84, v106, v107
	v_cvt_pk_bf16_f32 v85, v108, v109
	v_cvt_pk_bf16_f32 v78, v78, v79
	v_cvt_pk_bf16_f32 v79, v80, v81
	v_cvt_pk_bf16_f32 v80, v74, v75
	v_cvt_pk_bf16_f32 v81, v76, v77
	v_cvt_pk_bf16_f32 v74, v102, v103
	v_cvt_pk_bf16_f32 v75, v104, v105
	v_cvt_pk_bf16_f32 v76, v98, v99
	v_cvt_pk_bf16_f32 v77, v100, v101
	v_cvt_pk_bf16_f32 v73, v68, v69
	v_lshl_add_u64 v[58:59], v[58:59], 0, v[124:125]
	v_cvt_pk_bf16_f32 v49, v44, v45
	v_lshl_add_u64 v[60:61], v[42:43], 0, v[124:125]
	v_cvt_pk_bf16_f32 v42, v54, v55
	v_cvt_pk_bf16_f32 v43, v56, v57
	v_cvt_pk_bf16_f32 v44, v50, v51
	v_cvt_pk_bf16_f32 v45, v52, v53
	v_cvt_pk_bf16_f32 v30, v30, v31
	v_cvt_pk_bf16_f32 v31, v32, v33
	v_cvt_pk_bf16_f32 v32, v26, v27
	v_cvt_pk_bf16_f32 v33, v28, v29
	v_cvt_pk_bf16_f32 v26, v38, v39
	v_cvt_pk_bf16_f32 v27, v40, v41
	v_cvt_pk_bf16_f32 v28, v34, v35
	v_cvt_pk_bf16_f32 v29, v36, v37
	v_cvt_pk_bf16_f32 v14, v14, v15
	v_cvt_pk_bf16_f32 v15, v16, v17
	v_cvt_pk_bf16_f32 v16, v10, v11
	v_cvt_pk_bf16_f32 v17, v12, v13
	v_cvt_pk_bf16_f32 v10, v22, v23
	v_cvt_pk_bf16_f32 v11, v24, v25
	v_cvt_pk_bf16_f32 v12, v18, v19
	v_cvt_pk_bf16_f32 v13, v20, v21
	v_cvt_pk_bf16_f32 v6, v6, v7
	v_cvt_pk_bf16_f32 v7, v8, v9
	v_cvt_pk_bf16_f32 v8, v2, v3
	v_cvt_pk_bf16_f32 v9, v4, v5
	global_store_dwordx4 v[126:127], v[94:97], off nt
	global_store_dwordx4 v[122:123], v[90:93], off offset:512 nt
	global_store_dwordx4 v[126:127], v[86:89], off offset:512 nt
	global_store_dwordx4 v[122:123], v[82:85], off offset:1024 nt
	global_store_dwordx4 v[126:127], v[78:81], off offset:1024 nt
	global_store_dwordx4 v[122:123], v[74:77], off offset:1536 nt
	global_store_dwordx4 v[126:127], v[70:73], off offset:1536 nt
	global_store_dwordx4 v[58:59], v[62:65], off nt
	global_store_dwordx4 v[60:61], v[46:49], off nt
	global_store_dwordx4 v[58:59], v[42:45], off offset:512 nt
	global_store_dwordx4 v[60:61], v[30:33], off offset:512 nt
	global_store_dwordx4 v[58:59], v[26:29], off offset:1024 nt
	global_store_dwordx4 v[60:61], v[14:17], off offset:1024 nt
	global_store_dwordx4 v[58:59], v[10:13], off offset:1536 nt
	global_store_dwordx4 v[60:61], v[6:9], off offset:1536 nt
	s_branch .LBB0_229
